# packed v_pk_mul_f32 in rescale/finalize split into scalar v_mul_f32 (24 per head), bit-identical
# baseline (speedup 1.0000x reference)
.LBB1_47:
	v_max3_f32 v3, v1, v16, v14
	v_max3_f32 v3, v3, v15, v12
	v_max3_f32 v3, v3, v13, v9
	v_max_f32_e32 v3, v3, v11
	v_mov_b32_e32 v4, v3
	s_nop 1
	v_permlane32_swap_b32_e32 v3, v4
	v_max3_f32 v10, v236, v3, v4
	v_add_f32_e32 v244, s56, v10
	v_sub_f32_e32 v3, v236, v10
	v_exp_f32_e32 v4, v3
	s_nop 0
	v_mul_f32_e32 v82, v82, v4
	v_mul_f32_e32 v112, v4, v112
	v_mul_f32_e32 v113, v4, v113
	v_mul_f32_e32 v110, v4, v110
	v_mul_f32_e32 v111, v4, v111
	v_mul_f32_e32 v108, v4, v108
	v_mul_f32_e32 v109, v4, v109
	v_mul_f32_e32 v106, v4, v106
	v_mul_f32_e32 v107, v4, v107
	v_mul_f32_e32 v104, v4, v104
	v_mul_f32_e32 v105, v4, v105
	v_mul_f32_e32 v102, v4, v102
	v_mul_f32_e32 v103, v4, v103
	v_mul_f32_e32 v100, v4, v100
	v_mul_f32_e32 v101, v4, v101
	v_mul_f32_e32 v98, v4, v98
	v_mul_f32_e32 v99, v4, v99
	s_setprio 1
	v_cmp_lt_f32_e32 vcc, v244, v1
	s_cbranch_vccz .LBB1_86
	ds_read_b128 v[114:117], v206 offset:57344
	v_sub_f32_e32 v1, v66, v10
	v_sub_f32_e32 v3, v68, v10
	v_sub_f32_e32 v5, v70, v10
	v_sub_f32_e32 v7, v72, v10
	v_exp_f32_e32 v17, v1
	v_sub_f32_e32 v1, v67, v10
	v_exp_f32_e32 v4, v3
	v_sub_f32_e32 v3, v69, v10
	v_exp_f32_e32 v6, v5
	v_sub_f32_e32 v5, v71, v10
	v_exp_f32_e32 v8, v7
	v_sub_f32_e32 v7, v73, v10
	v_exp_f32_e32 v7, v7
	v_exp_f32_e32 v5, v5
	v_exp_f32_e32 v3, v3
	v_exp_f32_e32 v1, v1
	v_cvt_pk_f16_f32 v239, v8, v7
	v_cvt_pk_f16_f32 v238, v6, v5
	v_cvt_pk_f16_f32 v237, v4, v3
	v_cvt_pk_f16_f32 v236, v17, v1
	s_waitcnt lgkmcnt(0)
	s_nop 0
	v_mfma_f32_32x32x16_f16 v[98:113], v[114:117], v[236:239], v[98:113]
	v_mfma_f32_32x32x16_f16 v[82:97], v[194:197], v[236:239], v[82:97]
	v_cmp_lt_f32_e32 vcc, v244, v16
	s_cbranch_vccz .LBB1_50

.LBB1_59:
	s_setprio 0
	s_nop 10
	v_rcp_f32_e32 v8, v82
	v_cvt_f32_f16_sdwa v5, v229 dst_sel:DWORD dst_unused:UNUSED_PAD src0_sel:WORD_1
	v_cvt_f32_f16_e32 v4, v229
	v_cvt_f32_f16_sdwa v7, v230 dst_sel:DWORD dst_unused:UNUSED_PAD src0_sel:WORD_1
	v_cvt_f32_f16_e32 v6, v230
	v_cvt_f32_f16_sdwa v11, v232 dst_sel:DWORD dst_unused:UNUSED_PAD src0_sel:WORD_1
	v_cvt_f32_f16_e32 v10, v232
	v_cvt_f32_f16_sdwa v13, v234 dst_sel:DWORD dst_unused:UNUSED_PAD src0_sel:WORD_1
	v_cvt_f32_f16_e32 v12, v234
	v_mul_f32_e32 v4, v8, v4
	v_mul_f32_e32 v5, v8, v5
	v_mul_f32_e32 v6, v8, v6
	v_mul_f32_e32 v7, v8, v7
	v_mul_f32_e32 v4, v98, v4
	v_mul_f32_e32 v5, v99, v5
	v_mul_f32_e32 v6, v100, v6
	v_mul_f32_e32 v7, v101, v7
	v_cvt_pk_f16_f32 v4, v4, v5
	v_cvt_pk_f16_f32 v5, v6, v7
	v_mul_f32_e32 v6, v8, v10
	v_mul_f32_e32 v7, v8, v11
	v_mul_f32_e32 v10, v8, v12
	v_mul_f32_e32 v11, v8, v13
	v_mul_f32_e32 v6, v102, v6
	v_mul_f32_e32 v7, v103, v7
	v_mul_f32_e32 v10, v104, v10
	v_mul_f32_e32 v11, v105, v11
	v_cvt_pk_f16_f32 v6, v6, v7
	v_cvt_pk_f16_f32 v7, v10, v11
	v_cvt_f32_f16_sdwa v11, v228 dst_sel:DWORD dst_unused:UNUSED_PAD src0_sel:WORD_1
	v_cvt_f32_f16_e32 v10, v228
	ds_write_b128 v227, v[4:7]
	v_cvt_f32_f16_sdwa v7, v231 dst_sel:DWORD dst_unused:UNUSED_PAD src0_sel:WORD_1
	v_cvt_f32_f16_e32 v6, v231
	v_mul_f32_e32 v4, v8, v10
	v_mul_f32_e32 v5, v8, v11
	v_cvt_f32_f16_sdwa v11, v233 dst_sel:DWORD dst_unused:UNUSED_PAD src0_sel:WORD_1
	v_cvt_f32_f16_e32 v10, v233
	v_cvt_f32_f16_sdwa v13, v235 dst_sel:DWORD dst_unused:UNUSED_PAD src0_sel:WORD_1
	v_cvt_f32_f16_e32 v12, v235
	v_mul_f32_e32 v6, v8, v6
	v_mul_f32_e32 v7, v8, v7
	v_mul_f32_e32 v4, v4, v106
	v_mul_f32_e32 v5, v5, v107
	v_mul_f32_e32 v6, v6, v108
	v_mul_f32_e32 v7, v7, v109
	v_cvt_pk_f16_f32 v4, v4, v5
	v_cvt_pk_f16_f32 v5, v6, v7
	v_mul_f32_e32 v6, v8, v10
	v_mul_f32_e32 v7, v8, v11
	v_mul_f32_e32 v9, v8, v13
	v_mul_f32_e32 v8, v8, v12
	v_mul_f32_e32 v6, v6, v110
	v_mul_f32_e32 v7, v7, v111
	v_mul_f32_e32 v8, v8, v112
	v_mul_f32_e32 v9, v9, v113
	v_cvt_pk_f16_f32 v6, v6, v7
	v_cvt_pk_f16_f32 v7, v8, v9
	s_and_b64 vcc, exec, s[16:17]
	ds_write_b128 v227, v[4:7] offset:1024
	s_waitcnt vmcnt(0) lgkmcnt(2)
	s_barrier
	s_cbranch_vccnz .LBB1_5
	ds_read_b128 v[4:7], v206 offset:8192
	ds_read_b128 v[8:11], v206 offset:9216
	s_waitcnt lgkmcnt(1)
	v_mfma_f32_32x32x16_f16 v[114:129], v[4:7], v[130:133], 0
	ds_read_b128 v[4:7], v206 offset:16384
	ds_read_b128 v[12:15], v206 offset:17408
	s_waitcnt lgkmcnt(1)
	v_mfma_f32_32x32x16_f16 v[98:113], v[130:133], v[4:7], 0
	v_mfma_f32_32x32x16_f16 v[114:129], v[8:11], v[134:137], v[114:129]
	ds_read_b128 v[4:7], v206 offset:10240
	ds_read_b128 v[8:11], v206 offset:11264
	s_waitcnt lgkmcnt(2)
	v_mfma_f32_32x32x16_f16 v[98:113], v[134:137], v[12:15], v[98:113]
	s_waitcnt lgkmcnt(1)
	v_mfma_f32_32x32x16_f16 v[114:129], v[4:7], v[138:141], v[114:129]
	ds_read_b128 v[4:7], v206 offset:18432
	ds_read_b128 v[12:15], v206 offset:19456
	s_waitcnt lgkmcnt(1)
	v_mfma_f32_32x32x16_f16 v[98:113], v[138:141], v[4:7], v[98:113]
	v_mfma_f32_32x32x16_f16 v[114:129], v[8:11], v[142:145], v[114:129]
	ds_read_b128 v[4:7], v206 offset:12288
	ds_read_b128 v[8:11], v206 offset:13312
	s_waitcnt lgkmcnt(2)
	v_mfma_f32_32x32x16_f16 v[98:113], v[142:145], v[12:15], v[98:113]
	s_waitcnt lgkmcnt(1)
	v_mfma_f32_32x32x16_f16 v[114:129], v[4:7], v[146:149], v[114:129]
	ds_read_b128 v[4:7], v206 offset:20480
	ds_read_b128 v[12:15], v206 offset:21504
	s_waitcnt lgkmcnt(1)
	v_mfma_f32_32x32x16_f16 v[98:113], v[146:149], v[4:7], v[98:113]
	v_mfma_f32_32x32x16_f16 v[114:129], v[8:11], v[150:153], v[114:129]
	ds_read_b128 v[4:7], v206 offset:14336
	ds_read_b128 v[8:11], v206 offset:15360
	s_waitcnt lgkmcnt(2)
	v_mfma_f32_32x32x16_f16 v[98:113], v[150:153], v[12:15], v[98:113]
	s_waitcnt lgkmcnt(1)
	v_mfma_f32_32x32x16_f16 v[114:129], v[4:7], v[154:157], v[114:129]
	ds_read_b128 v[4:7], v206 offset:22528
	ds_read_b128 v[12:15], v206 offset:23552
	s_waitcnt lgkmcnt(1)
	v_mfma_f32_32x32x16_f16 v[98:113], v[154:157], v[4:7], v[98:113]
	v_mfma_f32_32x32x16_f16 v[114:129], v[8:11], v[158:161], v[114:129]
	ds_read_b128 v[4:7], v206 offset:24576
	ds_read_b128 v[8:11], v206 offset:25600
	s_waitcnt lgkmcnt(1)
	v_mfma_f32_32x32x16_f16 v[82:97], v[4:7], v[130:133], 0
	global_load_dwordx4 v[4:7], v[220:221], off
	s_nop 6
	v_cvt_pk_f16_f32 v121, v120, v121
	v_cvt_pk_f16_f32 v120, v118, v119
	v_cvt_pk_f16_f32 v119, v116, v117
	v_cvt_pk_f16_f32 v118, v114, v115
	v_cvt_pk_f16_f32 v117, v128, v129
	v_cvt_pk_f16_f32 v116, v126, v127
	s_waitcnt lgkmcnt(0)
	v_mfma_f32_32x32x16_f16 v[82:97], v[8:11], v[134:137], v[82:97]
	v_cvt_pk_f16_f32 v115, v124, v125
	v_cvt_pk_f16_f32 v114, v122, v123
	v_mfma_f32_32x32x16_f16 v[98:113], v[158:161], v[12:15], v[98:113]
	ds_read_b128 v[8:11], v206 offset:26624
	ds_read_b128 v[12:15], v206 offset:27648
	ds_read_b128 v[196:199], v206 offset:28672
	ds_write_b128 v209, v[114:117] offset:33792
	global_load_dwordx4 v[114:117], v[220:221], off offset:96
	ds_write_b128 v209, v[118:121] offset:32768
	ds_read_b128 v[118:121], v206 offset:29696
	s_nop 4
	v_cvt_pk_f16_f32 v105, v104, v105
	s_waitcnt lgkmcnt(5)
	v_mfma_f32_32x32x16_f16 v[82:97], v[8:11], v[138:141], v[82:97]
	global_load_dwordx4 v[8:11], v[220:221], off offset:32
	v_cvt_pk_f16_f32 v104, v102, v103
	v_cvt_pk_f16_f32 v103, v100, v101
	v_cvt_pk_f16_f32 v102, v98, v99
	ds_read_b128 v[98:101], v206 offset:30720
	ds_write_b128 v209, v[102:105] offset:49152
	v_cvt_pk_f16_f32 v103, v108, v109
	s_waitcnt lgkmcnt(6)
	v_mfma_f32_32x32x16_f16 v[82:97], v[12:15], v[142:145], v[82:97]
	global_load_dwordx4 v[12:15], v[220:221], off offset:64
	v_cvt_pk_f16_f32 v102, v106, v107
	ds_read_b128 v[106:109], v206 offset:31744
	v_cvt_pk_f16_f32 v105, v112, v113
	v_cvt_pk_f16_f32 v104, v110, v111
	ds_write_b128 v209, v[102:105] offset:50176
	s_waitcnt lgkmcnt(7)
	v_mfma_f32_32x32x16_f16 v[82:97], v[196:199], v[146:149], v[82:97]
	s_waitcnt lgkmcnt(4)
	v_mfma_f32_32x32x16_f16 v[82:97], v[118:121], v[150:153], v[82:97]
	s_waitcnt lgkmcnt(3)
	v_mfma_f32_32x32x16_f16 v[82:97], v[98:101], v[154:157], v[82:97]
	ds_read_b128 v[98:101], v206
	ds_read_b128 v[118:121], v206 offset:1024
	ds_read_b128 v[122:125], v206 offset:2048
	ds_read_b128 v[126:129], v206 offset:3072
	ds_read_b128 v[196:199], v206 offset:4096
	ds_read_b128 v[200:203], v206 offset:5120
	ds_read_b128 v[230:233], v206 offset:6144
	ds_read_b128 v[236:239], v206 offset:7168
	s_waitcnt lgkmcnt(0)
	s_barrier
	v_mfma_f32_32x32x16_f16 v[82:97], v[106:109], v[158:161], v[82:97]
	v_mfma_f32_32x32x16_f16 v[98:113], v[98:101], v[130:133], 0
	s_waitcnt vmcnt(3)
	s_nop 9
	v_add_f32_e32 v1, v82, v4
	v_mfma_f32_32x32x16_f16 v[98:113], v[118:121], v[134:137], v[98:113]
	v_add_f32_e32 v3, v5, v83
	v_add_f32_e32 v4, v6, v84
	v_add_f32_e32 v5, v7, v85
	v_mul_f32_e32 v1, 0xbfb8aa3b, v1
	v_mul_f32_e32 v3, 0xbfb8aa3b, v3
	v_mul_f32_e32 v4, 0xbfb8aa3b, v4
	v_mul_f32_e32 v5, 0xbfb8aa3b, v5
	v_mfma_f32_32x32x16_f16 v[98:113], v[122:125], v[138:141], v[98:113]
	v_exp_f32_e32 v1, v1
	v_exp_f32_e32 v3, v3
	v_exp_f32_e32 v4, v4
	v_exp_f32_e32 v5, v5
	v_add_f32_e32 v1, 1.0, v1
	v_add_f32_e32 v3, 1.0, v3
	v_add_f32_e32 v4, 1.0, v4
	v_mfma_f32_32x32x16_f16 v[98:113], v[126:129], v[142:145], v[98:113]
	v_add_f32_e32 v5, 1.0, v5
	s_waitcnt vmcnt(2)
	v_add_f32_e32 v16, v116, v96
	v_add_f32_e32 v17, v117, v97
	v_mul_f32_e32 v16, 0xbfb8aa3b, v16
	v_mul_f32_e32 v17, 0xbfb8aa3b, v17
	v_exp_f32_e32 v16, v16
	v_exp_f32_e32 v17, v17
	v_mfma_f32_32x32x16_f16 v[98:113], v[196:199], v[146:149], v[98:113]
	s_waitcnt vmcnt(1)
	v_add_f32_e32 v6, v86, v8
	v_add_f32_e32 v7, v9, v87
	v_add_f32_e32 v8, v10, v88
	v_add_f32_e32 v9, v11, v89
	v_mul_f32_e32 v6, 0xbfb8aa3b, v6
	v_mul_f32_e32 v7, 0xbfb8aa3b, v7
	v_mul_f32_e32 v8, 0xbfb8aa3b, v8
	v_mfma_f32_32x32x16_f16 v[98:113], v[200:203], v[150:153], v[98:113]
	s_waitcnt vmcnt(0)
	v_add_f32_e32 v10, v90, v12
	v_add_f32_e32 v11, v13, v91
	v_add_f32_e32 v12, v14, v92
	v_add_f32_e32 v13, v15, v93
	v_add_f32_e32 v14, v94, v114
	v_add_f32_e32 v15, v115, v95
	v_mul_f32_e32 v9, 0xbfb8aa3b, v9
	v_mfma_f32_32x32x16_f16 v[98:113], v[230:233], v[154:157], v[98:113]
	v_mul_f32_e32 v10, 0xbfb8aa3b, v10
	v_mul_f32_e32 v11, 0xbfb8aa3b, v11
	v_mul_f32_e32 v12, 0xbfb8aa3b, v12
	v_mul_f32_e32 v13, 0xbfb8aa3b, v13
	v_mul_f32_e32 v14, 0xbfb8aa3b, v14
	v_mul_f32_e32 v15, 0xbfb8aa3b, v15
	v_exp_f32_e32 v6, v6
	v_exp_f32_e32 v7, v7
	v_exp_f32_e32 v8, v8
	v_exp_f32_e32 v9, v9
	v_exp_f32_e32 v10, v10
	v_exp_f32_e32 v11, v11
	v_exp_f32_e32 v12, v12
	v_exp_f32_e32 v13, v13
	v_exp_f32_e32 v14, v14
	v_exp_f32_e32 v15, v15
	v_mfma_f32_32x32x16_f16 v[98:113], v[236:239], v[158:161], v[98:113]
	v_add_f32_e32 v6, 1.0, v6
	v_add_f32_e32 v7, 1.0, v7
	v_add_f32_e32 v8, 1.0, v8
	v_add_f32_e32 v9, 1.0, v9
	v_add_f32_e32 v10, 1.0, v10
	v_add_f32_e32 v11, 1.0, v11
	v_add_f32_e32 v12, 1.0, v12
	v_add_f32_e32 v13, 1.0, v13
	v_add_f32_e32 v14, 1.0, v14
	v_add_f32_e32 v15, 1.0, v15
	v_add_f32_e32 v16, 1.0, v16
	v_add_f32_e32 v17, 1.0, v17
	v_rcp_f32_e32 v1, v1
	v_rcp_f32_e32 v3, v3
	v_rcp_f32_e32 v4, v4
	v_rcp_f32_e32 v5, v5
	v_rcp_f32_e32 v6, v6
	v_rcp_f32_e32 v7, v7
	v_rcp_f32_e32 v8, v8
	v_rcp_f32_e32 v9, v9
	v_rcp_f32_e32 v10, v10
	v_rcp_f32_e32 v11, v11
	v_rcp_f32_e32 v12, v12
	v_rcp_f32_e32 v13, v13
	v_rcp_f32_e32 v14, v14
	v_rcp_f32_e32 v15, v15
	v_rcp_f32_e32 v16, v16
	v_rcp_f32_e32 v17, v17
	v_cvt_pk_f16_f32 v228, v10, v11
	v_cvt_pk_f16_f32 v231, v12, v13
	v_cvt_pk_f16_f32 v233, v14, v15
	v_cvt_pk_f16_f32 v235, v16, v17
	v_cvt_pk_f16_f32 v229, v1, v3
	v_cvt_pk_f16_f32 v230, v4, v5
	v_cvt_pk_f16_f32 v232, v6, v7
	v_cvt_pk_f16_f32 v234, v8, v9
	v_cvt_pk_f16_f32 v202, v106, v107
	v_cvt_pk_f16_f32 v203, v108, v109
	v_cvt_pk_f16_f32 v204, v110, v111
	v_cvt_pk_f16_f32 v205, v112, v113
	v_cvt_pk_f16_f32 v198, v98, v99
	v_cvt_pk_f16_f32 v199, v100, v101
	v_cvt_pk_f16_f32 v200, v102, v103
	v_cvt_pk_f16_f32 v201, v104, v105
	s_branch .LBB1_5
